# cache-policy: row pass A layer-1 X write-back stored non-temporally
# baseline (speedup 1.0000x reference)
.LBB0_382:
	v_readlane_b32 s10, v254, 8
	s_mov_b32 s12, 0xb00000
	s_mov_b32 s13, 0xa00000
	v_add_u32_e32 v62, s10, v68
	v_add_u32_e32 v64, s10, v87
	s_mov_b32 s10, 35
	s_ashr_i32 s11, s10, 31
	s_lshl_b64 s[10:11], s[10:11], 3
	s_add_u32 s10, s0, s10
	v_lshlrev_b32_e32 v63, 1, v62
	v_max_i32_e32 v62, v64, v62
	s_addc_u32 s11, s1, s11
	v_cmp_gt_i32_e32 vcc, s77, v62
	s_load_dwordx2 s[10:11], s[10:11], 0x0
	s_waitcnt vmcnt(3)
	v_ashrrev_i32_e32 v95, 31, v18
	v_cndmask_b32_e32 v62, v90, v63, vcc
	v_lshlrev_b32_e32 v74, 2, v62
	v_ashrrev_i32_e32 v75, 31, v74
	v_lshlrev_b64 v[62:63], 2, v[74:75]
	s_waitcnt lgkmcnt(0)
	v_lshl_add_u64 v[64:65], s[10:11], 0, v[62:63]
	s_mov_b32 s10, 35
	s_ashr_i32 s11, s10, 31
	s_lshl_b64 s[10:11], s[10:11], 3
	s_add_u32 s10, s0, s10
	s_addc_u32 s11, s1, s11
	s_load_dwordx2 s[10:11], s[10:11], 0x0
	v_or_b32_e32 v74, 4, v74
	v_ashrrev_i32_e32 v75, 31, v74
	v_lshlrev_b64 v[74:75], 2, v[74:75]
	v_mov_b32_e32 v94, v18
	s_waitcnt lgkmcnt(0)
	v_lshl_add_u64 v[66:67], s[10:11], 0, v[62:63]
	v_add_co_u32_e32 v62, vcc, s12, v64
	s_mov_b32 s10, 35
	s_nop 0
	v_addc_co_u32_e32 v63, vcc, 0, v65, vcc
	v_add_co_u32_e32 v66, vcc, s13, v66
	global_load_dwordx4 v[62:65], v[62:63], off
	s_nop 0
	v_addc_co_u32_e32 v67, vcc, 0, v67, vcc
	global_load_dwordx4 v[66:69], v[66:67], off
	s_ashr_i32 s11, s10, 31
	s_lshl_b64 s[10:11], s[10:11], 3
	s_add_u32 s10, s0, s10
	s_addc_u32 s11, s1, s11
	s_load_dwordx2 s[10:11], s[10:11], 0x0
	v_lshlrev_b64 v[94:95], 10, v[94:95]
	v_mov_b32_e32 v85, v1
	s_mov_b64 s[14:15], 0x48800000
	v_lshl_add_u32 v140, v100, 12, v89
	s_waitcnt lgkmcnt(0)
	v_lshl_add_u64 v[76:77], s[10:11], 0, v[74:75]
	s_mov_b32 s10, 35
	s_ashr_i32 s11, s10, 31
	s_lshl_b64 s[10:11], s[10:11], 3
	s_add_u32 s10, s0, s10
	s_addc_u32 s11, s1, s11
	s_load_dwordx2 s[10:11], s[10:11], 0x0
	s_waitcnt lgkmcnt(0)
	v_lshl_add_u64 v[78:79], s[10:11], 0, v[74:75]
	v_add_co_u32_e32 v74, vcc, s12, v76
	s_mov_b32 s10, 35
	s_nop 0
	v_addc_co_u32_e32 v75, vcc, 0, v77, vcc
	v_add_co_u32_e32 v78, vcc, s13, v78
	global_load_dwordx4 v[74:77], v[74:75], off
	s_nop 0
	v_addc_co_u32_e32 v79, vcc, 0, v79, vcc
	global_load_dwordx4 v[78:81], v[78:79], off
	s_ashr_i32 s11, s10, 31
	s_lshl_b64 s[10:11], s[10:11], 3
	s_add_u32 s10, s0, s10
	s_addc_u32 s11, s1, s11
	s_load_dwordx2 s[10:11], s[10:11], 0x0
	s_mov_b32 s12, 0x48800000
	s_waitcnt lgkmcnt(0)
	v_lshl_add_u64 v[94:95], s[10:11], 0, v[94:95]
	v_lshl_add_u64 v[94:95], v[94:95], 0, v[84:85]
	v_lshl_add_u64 v[96:97], v[94:95], 0, s[14:15]
	v_add_co_u32_e32 v94, vcc, s12, v94
	s_mov_b32 s10, 35
	s_nop 0
	v_addc_co_u32_e32 v95, vcc, 0, v95, vcc
	global_load_dword v118, v[94:95], off nt
	global_load_dword v130, v[96:97], off offset:256 nt
	global_load_dword v131, v[96:97], off offset:512 nt
	global_load_dword v112, v[96:97], off offset:768 nt
	s_ashr_i32 s11, s10, 31
	s_lshl_b64 s[10:11], s[10:11], 3
	s_add_u32 s10, s0, s10
	s_addc_u32 s11, s1, s11
	s_load_dwordx2 s[10:11], s[10:11], 0x0
	v_ashrrev_i32_e32 v95, 31, v19
	v_mov_b32_e32 v94, v19
	v_lshlrev_b64 v[94:95], 10, v[94:95]
	s_waitcnt lgkmcnt(0)
	v_lshl_add_u64 v[94:95], s[10:11], 0, v[94:95]
	v_lshl_add_u64 v[94:95], v[94:95], 0, v[84:85]
	v_lshl_add_u64 v[96:97], v[94:95], 0, s[14:15]
	v_add_co_u32_e32 v94, vcc, s12, v94
	s_mov_b32 s10, 35
	s_nop 0
	v_addc_co_u32_e32 v95, vcc, 0, v95, vcc
	global_load_dword v121, v[94:95], off nt
	global_load_dword v132, v[96:97], off offset:256 nt
	global_load_dword v133, v[96:97], off offset:512 nt
	global_load_dword v113, v[96:97], off offset:768 nt
	s_ashr_i32 s11, s10, 31
	s_lshl_b64 s[10:11], s[10:11], 3
	s_add_u32 s10, s0, s10
	s_addc_u32 s11, s1, s11
	s_load_dwordx2 s[10:11], s[10:11], 0x0
	v_ashrrev_i32_e32 v95, 31, v20
	v_mov_b32_e32 v94, v20
	v_lshlrev_b64 v[94:95], 10, v[94:95]
	s_waitcnt lgkmcnt(0)
	v_lshl_add_u64 v[94:95], s[10:11], 0, v[94:95]
	v_lshl_add_u64 v[94:95], v[94:95], 0, v[84:85]
	v_lshl_add_u64 v[96:97], v[94:95], 0, s[14:15]
	v_add_co_u32_e32 v94, vcc, s12, v94
	s_mov_b32 s10, 35
	s_nop 0
	v_addc_co_u32_e32 v95, vcc, 0, v95, vcc
	global_load_dword v125, v[94:95], off nt
	global_load_dword v134, v[96:97], off offset:256 nt
	global_load_dword v135, v[96:97], off offset:512 nt
	global_load_dword v136, v[96:97], off offset:768 nt
	s_ashr_i32 s11, s10, 31
	s_lshl_b64 s[10:11], s[10:11], 3
	s_add_u32 s10, s0, s10
	s_addc_u32 s11, s1, s11
	s_load_dwordx2 s[10:11], s[10:11], 0x0
	v_ashrrev_i32_e32 v95, 31, v21
	v_mov_b32_e32 v94, v21
	v_lshlrev_b64 v[94:95], 10, v[94:95]
	s_waitcnt lgkmcnt(0)
	v_lshl_add_u64 v[94:95], s[10:11], 0, v[94:95]
	v_lshl_add_u64 v[94:95], v[94:95], 0, v[84:85]
	v_lshl_add_u64 v[96:97], v[94:95], 0, s[14:15]
	v_add_co_u32_e32 v94, vcc, s12, v94
	s_mov_b32 s10, 35
	s_nop 0
	v_addc_co_u32_e32 v95, vcc, 0, v95, vcc
	global_load_dword v129, v[94:95], off nt
	global_load_dword v137, v[96:97], off offset:256 nt
	global_load_dword v138, v[96:97], off offset:512 nt
	global_load_dword v139, v[96:97], off offset:768 nt
	s_ashr_i32 s11, s10, 31
	s_lshl_b64 s[10:11], s[10:11], 3
	s_add_u32 s10, s0, s10
	s_addc_u32 s11, s1, s11
	s_load_dwordx2 s[10:11], s[10:11], 0x0
	s_waitcnt vmcnt(21)
	v_ashrrev_i32_e32 v95, 31, v26
	v_mov_b32_e32 v94, v26
	v_lshlrev_b64 v[94:95], 10, v[94:95]
	s_waitcnt lgkmcnt(0)
	v_lshl_add_u64 v[94:95], s[10:11], 0, v[94:95]
	v_lshl_add_u64 v[94:95], v[94:95], 0, v[84:85]
	v_lshl_add_u64 v[102:103], v[94:95], 0, s[14:15]
	v_add_co_u32_e32 v94, vcc, s12, v94
	s_mov_b32 s10, 35
	s_nop 0
	v_addc_co_u32_e32 v95, vcc, 0, v95, vcc
	global_load_dword v107, v[94:95], off nt
	global_load_dword v104, v[102:103], off offset:256 nt
	global_load_dword v97, v[102:103], off offset:512 nt
	s_nop 0
	global_load_dword v94, v[102:103], off offset:768 nt
	s_ashr_i32 s11, s10, 31
	s_lshl_b64 s[10:11], s[10:11], 3
	s_add_u32 s10, s0, s10
	s_addc_u32 s11, s1, s11
	s_load_dwordx2 s[10:11], s[10:11], 0x0
	v_ashrrev_i32_e32 v103, 31, v27
	v_mov_b32_e32 v102, v27
	v_lshlrev_b64 v[102:103], 10, v[102:103]
	s_waitcnt lgkmcnt(0)
	v_lshl_add_u64 v[102:103], s[10:11], 0, v[102:103]
	v_lshl_add_u64 v[102:103], v[102:103], 0, v[84:85]
	v_lshl_add_u64 v[110:111], v[102:103], 0, s[14:15]
	v_add_co_u32_e32 v102, vcc, s12, v102
	s_mov_b32 s10, 35
	s_nop 0
	v_addc_co_u32_e32 v103, vcc, 0, v103, vcc
	global_load_dword v109, v[102:103], off nt
	global_load_dword v105, v[110:111], off offset:256 nt
	global_load_dword v101, v[110:111], off offset:512 nt
	global_load_dword v95, v[110:111], off offset:768 nt
	s_ashr_i32 s11, s10, 31
	s_lshl_b64 s[10:11], s[10:11], 3
	s_add_u32 s10, s0, s10
	s_addc_u32 s11, s1, s11
	s_load_dwordx2 s[10:11], s[10:11], 0x0
	v_ashrrev_i32_e32 v103, 31, v28
	v_mov_b32_e32 v102, v28
	v_lshlrev_b64 v[102:103], 10, v[102:103]
	s_waitcnt vmcnt(19)
	v_cvt_f32_fp8_sdwa v119, v121 src0_sel:BYTE_1
	s_waitcnt lgkmcnt(0)
	v_lshl_add_u64 v[102:103], s[10:11], 0, v[102:103]
	v_lshl_add_u64 v[102:103], v[102:103], 0, v[84:85]
	v_lshl_add_u64 v[114:115], v[102:103], 0, s[14:15]
	v_add_co_u32_e32 v102, vcc, s12, v102
	s_mov_b32 s10, 35
	s_nop 0
	v_addc_co_u32_e32 v103, vcc, 0, v103, vcc
	global_load_dword v110, v[102:103], off nt
	global_load_dword v106, v[114:115], off offset:256 nt
	s_nop 0
	global_load_dword v102, v[114:115], off offset:512 nt
	global_load_dword v96, v[114:115], off offset:768 nt
	s_ashr_i32 s11, s10, 31
	s_lshl_b64 s[10:11], s[10:11], 3
	s_add_u32 s10, s0, s10
	s_addc_u32 s11, s1, s11
	s_load_dwordx2 s[10:11], s[10:11], 0x0
	v_ashrrev_i32_e32 v115, 31, v29
	v_mov_b32_e32 v114, v29
	v_lshlrev_b64 v[114:115], 10, v[114:115]
	v_cvt_f32_fp8_sdwa v120, v121 src0_sel:BYTE_2
	s_waitcnt lgkmcnt(0)
	v_lshl_add_u64 v[114:115], s[10:11], 0, v[114:115]
	v_lshl_add_u64 v[114:115], v[114:115], 0, v[84:85]
	v_lshl_add_u64 v[116:117], v[114:115], 0, s[14:15]
	v_add_co_u32_e32 v114, vcc, s12, v114
	s_waitcnt vmcnt(19)
	v_cvt_f32_fp8_e32 v122, v125
	v_addc_co_u32_e32 v115, vcc, 0, v115, vcc
	global_load_dword v111, v[114:115], off nt
	global_load_dword v108, v[116:117], off offset:256 nt
	global_load_dword v103, v[116:117], off offset:512 nt
	global_load_dword v85, v[116:117], off offset:768 nt
	v_cvt_f32_fp8_e32 v114, v118
	v_cvt_f32_fp8_sdwa v115, v118 src0_sel:BYTE_1
	v_cvt_f32_fp8_sdwa v116, v118 src0_sel:BYTE_2
	v_cvt_f32_fp8_sdwa v117, v118 src0_sel:BYTE_3
	v_cvt_f32_fp8_e32 v118, v121
	v_cvt_f32_fp8_sdwa v121, v121 src0_sel:BYTE_3
	v_cvt_f32_fp8_sdwa v123, v125 src0_sel:BYTE_1
	v_cvt_f32_fp8_sdwa v124, v125 src0_sel:BYTE_2
	v_cvt_f32_fp8_sdwa v125, v125 src0_sel:BYTE_3
	s_waitcnt vmcnt(19)
	v_cvt_f32_fp8_e32 v126, v129
	v_cvt_f32_fp8_sdwa v127, v129 src0_sel:BYTE_1
	v_cvt_f32_fp8_sdwa v128, v129 src0_sel:BYTE_2
	v_cvt_f32_fp8_sdwa v129, v129 src0_sel:BYTE_3
	v_pk_fma_f32 v[114:115], v[22:23], v[114:115], 0 op_sel_hi:[0,1,0]
	v_pk_fma_f32 v[116:117], v[22:23], v[116:117], 0 op_sel_hi:[0,1,0]
	v_pk_fma_f32 v[116:117], v[22:23], v[120:121], v[116:117] op_sel:[1,0,0]
	v_pk_fma_f32 v[114:115], v[22:23], v[118:119], v[114:115] op_sel:[1,0,0]
	v_pk_fma_f32 v[116:117], v[24:25], v[124:125], v[116:117] op_sel_hi:[0,1,1]
	v_pk_fma_f32 v[114:115], v[24:25], v[122:123], v[114:115] op_sel_hi:[0,1,1]
	v_pk_fma_f32 v[118:119], v[24:25], v[128:129], v[116:117] op_sel:[1,0,0]
	v_pk_fma_f32 v[120:121], v[24:25], v[126:127], v[114:115] op_sel:[1,0,0]
	ds_read_b128 v[114:117], v140
	v_cvt_f32_fp8_e32 v122, v134
	v_cvt_f32_fp8_sdwa v123, v134 src0_sel:BYTE_1
	v_cvt_f32_fp8_sdwa v124, v134 src0_sel:BYTE_2
	v_cvt_f32_fp8_sdwa v125, v134 src0_sel:BYTE_3
	s_waitcnt lgkmcnt(0)
	v_pk_fma_f32 v[70:71], v[114:115], v[120:121], v[70:71]
	v_pk_fma_f32 v[72:73], v[116:117], v[118:119], v[72:73]
	v_cvt_f32_fp8_e32 v114, v130
	v_cvt_f32_fp8_sdwa v115, v130 src0_sel:BYTE_1
	v_cvt_f32_fp8_sdwa v116, v130 src0_sel:BYTE_2
	v_cvt_f32_fp8_sdwa v117, v130 src0_sel:BYTE_3
	v_cvt_f32_fp8_e32 v118, v132
	v_cvt_f32_fp8_sdwa v119, v132 src0_sel:BYTE_1
	v_cvt_f32_fp8_sdwa v120, v132 src0_sel:BYTE_2
	v_cvt_f32_fp8_sdwa v121, v132 src0_sel:BYTE_3
	s_waitcnt vmcnt(18)
	v_cvt_f32_fp8_e32 v126, v137
	v_cvt_f32_fp8_sdwa v127, v137 src0_sel:BYTE_1
	v_cvt_f32_fp8_sdwa v128, v137 src0_sel:BYTE_2
	v_cvt_f32_fp8_sdwa v129, v137 src0_sel:BYTE_3
	v_pk_fma_f32 v[114:115], v[22:23], v[114:115], 0 op_sel_hi:[0,1,0]
	v_pk_fma_f32 v[116:117], v[22:23], v[116:117], 0 op_sel_hi:[0,1,0]
	v_pk_fma_f32 v[116:117], v[22:23], v[120:121], v[116:117] op_sel:[1,0,0]
	v_pk_fma_f32 v[114:115], v[22:23], v[118:119], v[114:115] op_sel:[1,0,0]
	v_pk_fma_f32 v[116:117], v[24:25], v[124:125], v[116:117] op_sel_hi:[0,1,1]
	v_pk_fma_f32 v[114:115], v[24:25], v[122:123], v[114:115] op_sel_hi:[0,1,1]
	v_pk_fma_f32 v[118:119], v[24:25], v[128:129], v[116:117] op_sel:[1,0,0]
	v_pk_fma_f32 v[120:121], v[24:25], v[126:127], v[114:115] op_sel:[1,0,0]
	ds_read_b128 v[114:117], v140 offset:1024
	v_cvt_f32_fp8_e32 v122, v135
	v_cvt_f32_fp8_sdwa v123, v135 src0_sel:BYTE_1
	v_cvt_f32_fp8_sdwa v124, v135 src0_sel:BYTE_2
	v_cvt_f32_fp8_sdwa v125, v135 src0_sel:BYTE_3
	s_waitcnt lgkmcnt(0)
	v_pk_fma_f32 v[58:59], v[114:115], v[120:121], v[58:59]
	v_pk_fma_f32 v[60:61], v[116:117], v[118:119], v[60:61]
	v_cvt_f32_fp8_e32 v114, v131
	v_cvt_f32_fp8_sdwa v115, v131 src0_sel:BYTE_1
	v_cvt_f32_fp8_sdwa v116, v131 src0_sel:BYTE_2
	v_cvt_f32_fp8_sdwa v117, v131 src0_sel:BYTE_3
	v_cvt_f32_fp8_e32 v118, v133
	v_cvt_f32_fp8_sdwa v119, v133 src0_sel:BYTE_1
	v_cvt_f32_fp8_sdwa v120, v133 src0_sel:BYTE_2
	v_cvt_f32_fp8_sdwa v121, v133 src0_sel:BYTE_3
	s_waitcnt vmcnt(17)
	v_cvt_f32_fp8_e32 v126, v138
	v_cvt_f32_fp8_sdwa v127, v138 src0_sel:BYTE_1
	v_cvt_f32_fp8_sdwa v128, v138 src0_sel:BYTE_2
	v_cvt_f32_fp8_sdwa v129, v138 src0_sel:BYTE_3
	v_pk_fma_f32 v[114:115], v[22:23], v[114:115], 0 op_sel_hi:[0,1,0]
	v_pk_fma_f32 v[116:117], v[22:23], v[116:117], 0 op_sel_hi:[0,1,0]
	v_pk_fma_f32 v[116:117], v[22:23], v[120:121], v[116:117] op_sel:[1,0,0]
	v_pk_fma_f32 v[114:115], v[22:23], v[118:119], v[114:115] op_sel:[1,0,0]
	v_pk_fma_f32 v[116:117], v[24:25], v[124:125], v[116:117] op_sel_hi:[0,1,1]
	v_pk_fma_f32 v[114:115], v[24:25], v[122:123], v[114:115] op_sel_hi:[0,1,1]
	v_pk_fma_f32 v[118:119], v[24:25], v[128:129], v[116:117] op_sel:[1,0,0]
	v_pk_fma_f32 v[120:121], v[24:25], v[126:127], v[114:115] op_sel:[1,0,0]
	ds_read_b128 v[114:117], v140 offset:2048
	v_cvt_f32_fp8_sdwa v122, v136 src0_sel:BYTE_2
	v_cvt_f32_fp8_sdwa v123, v136 src0_sel:BYTE_3
	s_waitcnt vmcnt(16)
	v_cvt_f32_fp8_e32 v124, v139
	v_cvt_f32_fp8_sdwa v125, v139 src0_sel:BYTE_1
	s_waitcnt lgkmcnt(0)
	v_pk_fma_f32 v[54:55], v[114:115], v[120:121], v[54:55]
	v_pk_fma_f32 v[56:57], v[116:117], v[118:119], v[56:57]
	v_cvt_f32_fp8_e32 v114, v112
	v_cvt_f32_fp8_sdwa v115, v112 src0_sel:BYTE_1
	v_cvt_f32_fp8_sdwa v116, v112 src0_sel:BYTE_2
	v_cvt_f32_fp8_sdwa v117, v112 src0_sel:BYTE_3
	v_cvt_f32_fp8_e32 v118, v113
	v_cvt_f32_fp8_sdwa v119, v113 src0_sel:BYTE_1
	v_cvt_f32_fp8_sdwa v112, v113 src0_sel:BYTE_2
	v_cvt_f32_fp8_sdwa v113, v113 src0_sel:BYTE_3
	v_cvt_f32_fp8_e32 v120, v136
	v_cvt_f32_fp8_sdwa v121, v136 src0_sel:BYTE_1
	v_cvt_f32_fp8_sdwa v126, v139 src0_sel:BYTE_2
	v_cvt_f32_fp8_sdwa v127, v139 src0_sel:BYTE_3
	v_pk_fma_f32 v[114:115], v[22:23], v[114:115], 0 op_sel_hi:[0,1,0]
	v_pk_fma_f32 v[116:117], v[22:23], v[116:117], 0 op_sel_hi:[0,1,0]
	v_pk_fma_f32 v[112:113], v[22:23], v[112:113], v[116:117] op_sel:[1,0,0]
	v_pk_fma_f32 v[114:115], v[22:23], v[118:119], v[114:115] op_sel:[1,0,0]
	v_pk_fma_f32 v[112:113], v[24:25], v[122:123], v[112:113] op_sel_hi:[0,1,1]
	v_pk_fma_f32 v[114:115], v[24:25], v[120:121], v[114:115] op_sel_hi:[0,1,1]
	v_pk_fma_f32 v[116:117], v[24:25], v[126:127], v[112:113] op_sel:[1,0,0]
	v_pk_fma_f32 v[118:119], v[24:25], v[124:125], v[114:115] op_sel:[1,0,0]
	ds_read_b128 v[112:115], v140 offset:3072
	s_waitcnt vmcnt(7)
	v_cvt_f32_fp8_e32 v120, v110
	v_cvt_f32_fp8_sdwa v121, v110 src0_sel:BYTE_1
	v_cvt_f32_fp8_sdwa v122, v110 src0_sel:BYTE_2
	v_cvt_f32_fp8_sdwa v123, v110 src0_sel:BYTE_3
	s_waitcnt lgkmcnt(0)
	v_pk_fma_f32 v[42:43], v[112:113], v[118:119], v[42:43]
	v_pk_fma_f32 v[44:45], v[114:115], v[116:117], v[44:45]
	v_cvt_f32_fp8_e32 v112, v107
	v_cvt_f32_fp8_sdwa v113, v107 src0_sel:BYTE_1
	v_cvt_f32_fp8_sdwa v114, v107 src0_sel:BYTE_2
	v_cvt_f32_fp8_sdwa v115, v107 src0_sel:BYTE_3
	v_cvt_f32_fp8_e32 v116, v109
	v_cvt_f32_fp8_sdwa v117, v109 src0_sel:BYTE_1
	v_cvt_f32_fp8_sdwa v118, v109 src0_sel:BYTE_2
	v_cvt_f32_fp8_sdwa v119, v109 src0_sel:BYTE_3
	s_waitcnt vmcnt(3)
	v_cvt_f32_fp8_e32 v124, v111
	v_cvt_f32_fp8_sdwa v125, v111 src0_sel:BYTE_1
	v_cvt_f32_fp8_sdwa v110, v111 src0_sel:BYTE_2
	v_cvt_f32_fp8_sdwa v111, v111 src0_sel:BYTE_3
	v_pk_fma_f32 v[114:115], v[30:31], v[114:115], 0 op_sel_hi:[0,1,0]
	v_pk_fma_f32 v[112:113], v[30:31], v[112:113], 0 op_sel_hi:[0,1,0]
	v_pk_fma_f32 v[112:113], v[30:31], v[116:117], v[112:113] op_sel:[1,0,0]
	v_pk_fma_f32 v[114:115], v[30:31], v[118:119], v[114:115] op_sel:[1,0,0]
	v_lshl_add_u32 v126, v99, 12, v89
	v_pk_fma_f32 v[114:115], v[32:33], v[122:123], v[114:115] op_sel_hi:[0,1,1]
	v_pk_fma_f32 v[112:113], v[32:33], v[120:121], v[112:113] op_sel_hi:[0,1,1]
	v_pk_fma_f32 v[116:117], v[32:33], v[124:125], v[112:113] op_sel:[1,0,0]
	v_pk_fma_f32 v[114:115], v[32:33], v[110:111], v[114:115] op_sel:[1,0,0]
	ds_read_b128 v[110:113], v126
	v_cvt_f32_fp8_sdwa v118, v106 src0_sel:BYTE_2
	v_cvt_f32_fp8_sdwa v119, v106 src0_sel:BYTE_3
	s_waitcnt vmcnt(2)
	v_cvt_f32_fp8_sdwa v107, v108 src0_sel:BYTE_1
	v_cvt_f32_fp8_sdwa v120, v108 src0_sel:BYTE_2
	s_waitcnt lgkmcnt(0)
	v_pk_fma_f32 v[52:53], v[112:113], v[114:115], v[52:53]
	v_pk_fma_f32 v[50:51], v[110:111], v[116:117], v[50:51]
	v_cvt_f32_fp8_e32 v110, v104
	v_cvt_f32_fp8_sdwa v111, v104 src0_sel:BYTE_1
	v_cvt_f32_fp8_sdwa v112, v104 src0_sel:BYTE_2
	v_cvt_f32_fp8_sdwa v113, v104 src0_sel:BYTE_3
	v_cvt_f32_fp8_e32 v114, v105
	v_cvt_f32_fp8_sdwa v115, v105 src0_sel:BYTE_1
	v_cvt_f32_fp8_sdwa v104, v105 src0_sel:BYTE_2
	v_cvt_f32_fp8_sdwa v105, v105 src0_sel:BYTE_3
	v_cvt_f32_fp8_e32 v116, v106
	v_cvt_f32_fp8_sdwa v117, v106 src0_sel:BYTE_1
	v_cvt_f32_fp8_e32 v106, v108
	v_cvt_f32_fp8_sdwa v121, v108 src0_sel:BYTE_3
	v_pk_fma_f32 v[108:109], v[30:31], v[112:113], 0 op_sel_hi:[0,1,0]
	v_pk_fma_f32 v[110:111], v[30:31], v[110:111], 0 op_sel_hi:[0,1,0]
	v_pk_fma_f32 v[110:111], v[30:31], v[114:115], v[110:111] op_sel:[1,0,0]
	v_pk_fma_f32 v[104:105], v[30:31], v[104:105], v[108:109] op_sel:[1,0,0]
	v_pk_fma_f32 v[108:109], v[32:33], v[116:117], v[110:111] op_sel_hi:[0,1,1]
	v_pk_fma_f32 v[104:105], v[32:33], v[118:119], v[104:105] op_sel_hi:[0,1,1]
	v_pk_fma_f32 v[108:109], v[32:33], v[106:107], v[108:109] op_sel:[1,0,0]
	v_pk_fma_f32 v[110:111], v[32:33], v[120:121], v[104:105] op_sel:[1,0,0]
	ds_read_b128 v[104:107], v126 offset:1024
	v_cvt_f32_fp8_e32 v112, v102
	v_cvt_f32_fp8_sdwa v113, v102 src0_sel:BYTE_1
	v_cvt_f32_fp8_sdwa v114, v102 src0_sel:BYTE_2
	v_cvt_f32_fp8_sdwa v115, v102 src0_sel:BYTE_3
	s_waitcnt lgkmcnt(0)
	v_pk_fma_f32 v[48:49], v[106:107], v[110:111], v[48:49]
	v_pk_fma_f32 v[46:47], v[104:105], v[108:109], v[46:47]
	v_cvt_f32_fp8_e32 v104, v97
	v_cvt_f32_fp8_sdwa v105, v97 src0_sel:BYTE_1
	v_cvt_f32_fp8_sdwa v106, v97 src0_sel:BYTE_2
	v_cvt_f32_fp8_sdwa v107, v97 src0_sel:BYTE_3
	v_cvt_f32_fp8_e32 v108, v101
	v_cvt_f32_fp8_sdwa v109, v101 src0_sel:BYTE_1
	v_cvt_f32_fp8_sdwa v110, v101 src0_sel:BYTE_2
	v_cvt_f32_fp8_sdwa v111, v101 src0_sel:BYTE_3
	s_waitcnt vmcnt(1)
	v_cvt_f32_fp8_e32 v116, v103
	v_cvt_f32_fp8_sdwa v117, v103 src0_sel:BYTE_1
	v_cvt_f32_fp8_sdwa v102, v103 src0_sel:BYTE_2
	v_cvt_f32_fp8_sdwa v103, v103 src0_sel:BYTE_3
	v_pk_fma_f32 v[106:107], v[30:31], v[106:107], 0 op_sel_hi:[0,1,0]
	v_pk_fma_f32 v[104:105], v[30:31], v[104:105], 0 op_sel_hi:[0,1,0]
	v_pk_fma_f32 v[104:105], v[30:31], v[108:109], v[104:105] op_sel:[1,0,0]
	v_pk_fma_f32 v[106:107], v[30:31], v[110:111], v[106:107] op_sel:[1,0,0]
	v_pk_fma_f32 v[104:105], v[32:33], v[112:113], v[104:105] op_sel_hi:[0,1,1]
	v_pk_fma_f32 v[106:107], v[32:33], v[114:115], v[106:107] op_sel_hi:[0,1,1]
	v_pk_fma_f32 v[108:109], v[32:33], v[116:117], v[104:105] op_sel:[1,0,0]
	v_pk_fma_f32 v[106:107], v[32:33], v[102:103], v[106:107] op_sel:[1,0,0]
	ds_read_b128 v[102:105], v126 offset:2048
	v_cvt_f32_fp8_sdwa v110, v96 src0_sel:BYTE_2
	v_cvt_f32_fp8_sdwa v111, v96 src0_sel:BYTE_3
	s_waitcnt vmcnt(0)
	v_cvt_f32_fp8_sdwa v97, v85 src0_sel:BYTE_1
	v_cvt_f32_fp8_sdwa v112, v85 src0_sel:BYTE_2
	s_waitcnt lgkmcnt(0)
	v_pk_fma_f32 v[40:41], v[104:105], v[106:107], v[40:41]
	v_pk_fma_f32 v[38:39], v[102:103], v[108:109], v[38:39]
	v_cvt_f32_fp8_e32 v102, v94
	v_cvt_f32_fp8_sdwa v103, v94 src0_sel:BYTE_1
	v_cvt_f32_fp8_sdwa v104, v94 src0_sel:BYTE_2
	v_cvt_f32_fp8_sdwa v105, v94 src0_sel:BYTE_3
	v_cvt_f32_fp8_e32 v106, v95
	v_cvt_f32_fp8_sdwa v107, v95 src0_sel:BYTE_1
	v_cvt_f32_fp8_sdwa v94, v95 src0_sel:BYTE_2
	v_cvt_f32_fp8_sdwa v95, v95 src0_sel:BYTE_3
	v_cvt_f32_fp8_e32 v108, v96
	v_cvt_f32_fp8_sdwa v109, v96 src0_sel:BYTE_1
	v_cvt_f32_fp8_e32 v96, v85
	v_cvt_f32_fp8_sdwa v113, v85 src0_sel:BYTE_3
	v_pk_fma_f32 v[104:105], v[30:31], v[104:105], 0 op_sel_hi:[0,1,0]
	v_pk_fma_f32 v[102:103], v[30:31], v[102:103], 0 op_sel_hi:[0,1,0]
	v_pk_fma_f32 v[102:103], v[30:31], v[106:107], v[102:103] op_sel:[1,0,0]
	v_pk_fma_f32 v[94:95], v[30:31], v[94:95], v[104:105] op_sel:[1,0,0]
	v_pk_fma_f32 v[102:103], v[32:33], v[108:109], v[102:103] op_sel_hi:[0,1,1]
	v_pk_fma_f32 v[94:95], v[32:33], v[110:111], v[94:95] op_sel_hi:[0,1,1]
	v_pk_fma_f32 v[102:103], v[32:33], v[96:97], v[102:103] op_sel:[1,0,0]
	v_pk_fma_f32 v[104:105], v[32:33], v[112:113], v[94:95] op_sel:[1,0,0]
	ds_read_b128 v[94:97], v126 offset:3072
	v_cvt_pk_bf16_f32 v85, v70, v71
	v_cvt_pk_bf16_f32 v101, v72, v73
	v_mov_b32_e32 v106, v1
	v_mov_b32_e32 v107, v1
	s_waitcnt lgkmcnt(0)
	v_pk_fma_f32 v[36:37], v[96:97], v[104:105], v[36:37]
	v_cvt_pk_bf16_f32 v104, v58, v59
	v_pk_fma_f32 v[34:35], v[94:95], v[102:103], v[34:35]
	v_cvt_pk_bf16_f32 v105, v60, v61
	v_cndmask_b32_e64 v102, v85, v104, s[8:9]
	v_lshlrev_b64 v[96:97], 11, v[90:91]
	v_lshl_add_u64 v[94:95], s[18:19], 0, v[96:97]
	v_mov_b32_dpp v106, v102 quad_perm:[1,0,3,2] row_mask:0xf bank_mask:0xf
	v_cndmask_b32_e64 v102, v101, v105, s[8:9]
	v_cndmask_b32_e64 v104, v104, v106, s[8:9]
	v_mov_b32_e32 v112, v1
	v_mov_b32_dpp v107, v102 quad_perm:[1,0,3,2] row_mask:0xf bank_mask:0xf
	v_cndmask_b32_e64 v102, v106, v85, s[8:9]
	v_cndmask_b32_e64 v103, v107, v101, s[8:9]
	v_cndmask_b32_e64 v105, v105, v107, s[8:9]
	v_lshlrev_b32_e32 v106, 1, v86
	v_mov_b32_e32 v107, v1
	v_lshl_add_u64 v[108:109], v[94:95], 0, v[106:107]
	global_store_dwordx4 v[108:109], v[102:105], off nt
	v_cvt_pk_bf16_f32 v85, v54, v55
	v_cvt_pk_bf16_f32 v101, v56, v57
	v_cvt_pk_bf16_f32 v102, v42, v43
	v_cvt_pk_bf16_f32 v103, v44, v45
	v_cndmask_b32_e64 v104, v85, v102, s[8:9]
	v_mov_b32_e32 v105, v1
	v_mov_b32_e32 v108, v1
	v_mov_b32_e32 v109, v1
	v_mov_b32_dpp v105, v104 quad_perm:[1,0,3,2] row_mask:0xf bank_mask:0xf
	v_cndmask_b32_e64 v104, v101, v103, s[8:9]
	v_mov_b32_e32 v113, v1
	s_nop 0
	v_mov_b32_dpp v108, v104 quad_perm:[1,0,3,2] row_mask:0xf bank_mask:0xf
	v_cndmask_b32_e64 v104, v102, v105, s[8:9]
	v_cndmask_b32_e64 v102, v105, v85, s[8:9]
	v_cndmask_b32_e64 v105, v103, v108, s[8:9]
	v_cndmask_b32_e64 v103, v108, v101, s[8:9]
	v_lshlrev_b32_e32 v108, 1, v88
	v_lshl_add_u64 v[94:95], v[94:95], 0, v[108:109]
	global_store_dwordx4 v[94:95], v[102:105], off nt
	v_cvt_pk_bf16_f32 v85, v50, v51
	v_cvt_pk_bf16_f32 v101, v52, v53
	v_cvt_pk_bf16_f32 v104, v46, v47
	v_cvt_pk_bf16_f32 v105, v48, v49
	v_cndmask_b32_e64 v102, v85, v104, s[8:9]
	v_lshlrev_b64 v[94:95], 11, v[92:93]
	v_lshl_add_u64 v[110:111], s[18:19], 0, v[94:95]
	v_mov_b32_dpp v112, v102 quad_perm:[1,0,3,2] row_mask:0xf bank_mask:0xf
	v_cndmask_b32_e64 v102, v101, v105, s[8:9]
	v_cndmask_b32_e64 v104, v104, v112, s[8:9]
	v_lshl_add_u64 v[106:107], v[110:111], 0, v[106:107]
	v_mov_b32_dpp v113, v102 quad_perm:[1,0,3,2] row_mask:0xf bank_mask:0xf
	v_cndmask_b32_e64 v103, v113, v101, s[8:9]
	v_cndmask_b32_e64 v102, v112, v85, s[8:9]
	v_cndmask_b32_e64 v105, v105, v113, s[8:9]
	global_store_dwordx4 v[106:107], v[102:105], off nt
	v_cvt_pk_bf16_f32 v85, v38, v39
	v_cvt_pk_bf16_f32 v101, v40, v41
	v_cvt_pk_bf16_f32 v102, v34, v35
	v_cvt_pk_bf16_f32 v103, v36, v37
	v_cndmask_b32_e64 v104, v85, v102, s[8:9]
	v_mov_b32_e32 v106, v1
	v_mov_b32_e32 v107, v1
	s_nop 0
	v_mov_b32_dpp v106, v104 quad_perm:[1,0,3,2] row_mask:0xf bank_mask:0xf
	v_cndmask_b32_e64 v104, v101, v103, s[8:9]
	s_nop 1
	v_mov_b32_dpp v107, v104 quad_perm:[1,0,3,2] row_mask:0xf bank_mask:0xf
	v_cndmask_b32_e64 v105, v103, v107, s[8:9]
	v_cndmask_b32_e64 v104, v102, v106, s[8:9]
	v_cndmask_b32_e64 v103, v107, v101, s[8:9]
	v_cndmask_b32_e64 v102, v106, v85, s[8:9]
	v_lshl_add_u64 v[106:107], v[110:111], 0, v[108:109]
	global_store_dwordx4 v[106:107], v[102:105], off nt
	s_cbranch_execnz .LBB0_368
	s_branch .LBB0_367
